# P7 K-tile LDS swizzle made conflict-free for the ds_read_b128 lane groups (writer and reader changed together)
# baseline (speedup 1.0000x reference)
.Lp7prio:
	v_lshrrev_b32_e32 v1, 4, v0
	v_lshrrev_b32_e32 v9, 3, v0
	v_and_b32_e32 v9, 8, v9
	v_or_b32_e32 v15, 32, v1
	v_lshlrev_b32_e32 v5, 3, v0
	v_and_or_b32 v10, v1, 16, v9
	v_and_or_b32 v9, v15, 48, v9
	v_and_b32_e32 v7, 0x78, v5
	v_lshrrev_b32_e32 v11, 5, v0
	v_lshrrev_b32_e32 v10, 1, v10
	v_bfe_u32 v12, v5, 5, 2
	v_bfe_u32 v13, v0, 4, 2
	v_lshrrev_b32_e32 v9, 1, v9
	v_or_b32_e32 v10, v10, v12
	v_and_or_b32 v11, v11, 4, v13
	v_lshlrev_b32_e32 v13, 1, v7
	v_or_b32_e32 v9, v9, v12
	v_lshlrev_b32_e32 v10, 9, v10
	v_lshlrev_b32_e32 v11, 6, v11
	v_and_b32_e32 v14, 48, v13
	v_lshlrev_b32_e32 v9, 9, v9
	v_or3_b32 v10, v10, v11, v14
	v_or3_b32 v9, v9, v11, v14
	v_lshlrev_b32_e32 v11, 4, v0
	v_lshlrev_b32_e32 v14, 1, v0
	v_and_b32_e32 v12, 0xc0, v11
	v_and_b32_e32 v14, 32, v14
	v_and_b32_e32 v5, 0x118, v5
	v_or3_b32 v12, v14, v12, v5
	v_mul_u32_u24_e32 v14, 0x2700, v1
	v_or_b32_e32 v5, v14, v7
	v_bfe_u32 v6, v0, 5, 1
	s_waitcnt vmcnt(23)
	v_lshlrev_b32_e32 v150, 1, v5
	v_lshlrev_b32_e32 v1, 8, v1
	v_lshrrev_b32_e32 v5, 1, v0
	v_and_b32_e32 v5, 0xc0, v5
	v_and_or_b32 v5, v0, 48, v5
	s_movk_i32 s4, 0x70
	v_bitop3_b32 v16, v13, v1, v5 bitop3:0xde
	v_lshlrev_b32_e32 v1, 8, v15
	v_lshlrev_b32_e32 v15, 4, v6
	v_bitop3_b32 v13, v13, v1, v5 bitop3:0xde
	v_lshlrev_b32_e32 v1, 3, v0
	v_and_b32_e32 v1, 0xc0, v1
	v_and_or_b32 v1, v11, 48, v1
	v_xor_b32_e32 v11, v15, v1
	s_movk_i32 s4, 0x60
	s_waitcnt vmcnt(0)
	v_bitop3_b32 v19, v15, v1, s4 bitop3:0x36
	s_movk_i32 s4, 0x80
	s_add_u32 s10, s44, 0x49098000
	v_and_b32_e32 v146, 31, v2
	v_mov_b32_e32 v149, 0
	v_and_b32_e32 v3, 63, v0
	s_movk_i32 s3, 0xc0
	v_bitop3_b32 v20, v15, v1, s4 bitop3:0x36
	s_movk_i32 s4, 0xa0
	v_lshrrev_b32_e32 v2, 1, v2
	s_addc_u32 s11, s45, 0
	v_and_b32_e32 v4, 31, v0
	v_bitop3_b32 v21, v15, v1, s4 bitop3:0x36
	v_bitop3_b32 v22, v15, v1, s3 bitop3:0x36
	s_movk_i32 s3, 0xe0
	v_cmp_gt_u32_e64 s[4:5], 32, v3
	v_mov_b32_e32 v5, v149
	v_and_b32_e32 v2, 16, v2
	v_mov_b32_e32 v3, v149
	v_and_b32_e32 v8, 0x1c0, v0
	v_bitop3_b32 v17, v15, v1, 32 bitop3:0x36
	v_bitop3_b32 v18, v15, v1, 64 bitop3:0x36
	v_bitop3_b32 v23, v15, v1, s3 bitop3:0x36
	v_lshlrev_b32_e32 v1, 2, v6
	v_lshlrev_b32_e32 v6, 12, v6
	v_mov_b32_e32 v7, v149
	v_lshl_add_u64 v[154:155], s[10:11], 0, v[2:3]
	s_add_i32 s6, 0, 0x10000
	v_lshl_add_u64 v[2:3], s[44:45], 0, v[4:5]
	v_lshl_add_u32 v8, v8, 2, s6
	v_lshl_add_u64 v[2:3], v[2:3], 0, v[6:7]
	s_mov_b64 s[6:7], 0x9aa98000
	v_lshlrev_b32_e32 v148, 10, v4
	v_lshl_add_u64 v[156:157], v[2:3], 0, s[6:7]
	s_add_i32 s6, 0, 0x4000
	v_add_u32_e32 v197, s6, v12
	v_lshl_add_u64 v[2:3], s[44:45], 0, v[148:149]
	s_mov_b64 s[6:7], 0x98a98000
	s_lshl_b32 s3, s52, 5
	v_lshl_add_u32 v5, v4, 8, 0
	v_lshl_add_u64 v[158:159], v[2:3], 0, s[6:7]
	v_and_b32_e32 v2, 15, v0
	v_lshlrev_b32_e32 v3, 1, v14
	v_add_u32_e32 v152, 0x9c000, v150
	v_mov_b32_e32 v151, v149
	v_mov_b32_e32 v153, v149
	s_and_b32 s3, s3, 32
	s_and_b32 s19, s66, 0xffffff80
	s_mov_b32 s13, 0
	v_add_u32_e32 v147, 0, v12
	v_lshl_add_u32 v196, v4, 2, v8
	s_movk_i32 s30, 0x4000
	v_add_u32_e32 v198, v8, v15
	v_lshl_or_b32 v160, v2, 4, v3
	v_mov_b32_e32 v161, v149
	s_mov_b64 s[14:15], 0xa00
	s_mov_b64 s[16:17], 0x800
	s_movk_i32 s31, 0x4e00
	s_mov_b32 s34, 0xff800000
	s_mov_b32 s35, 0x42b504f3
	s_mov_b32 s18, 0x3e0293ee
	s_mov_b32 s36, 0x49308000
	s_mov_b32 s37, 0x493a4000
	s_mov_b32 s38, 0x49440000
	s_mov_b32 s39, 0x494dc000
	s_mov_b64 s[20:21], 0x270000
	s_mov_b32 s40, 0xc3e00000
	s_movk_i32 s41, 0x2000
	s_movk_i32 s42, 0x6000
	v_mov_b32_e32 v149, 0x4e00
	v_add_u32_e32 v199, 0, v10
	v_add_u32_e32 v200, 0, v9
	v_add_u32_e32 v201, 0, v16
	v_add_u32_e32 v202, 0, v13
	v_add_u32_e32 v203, v5, v11
	v_add_u32_e32 v204, v5, v17
	v_add_u32_e32 v205, v5, v18
	v_add_u32_e32 v206, v5, v19
	v_add_u32_e32 v207, v5, v20
	v_add_u32_e32 v208, v5, v21
	v_add_u32_e32 v209, v5, v22
	v_add_u32_e32 v210, v5, v23
	v_mov_b32_e32 v211, 0xf149f2ca
	v_mov_b32_e32 v212, 0x43e00000
	s_mov_b32 s43, s2
	s_branch .LBB0_1719
